# LN1 router-weight staging: the 8 serial load-wait-LDS-store iterations unrolled into 8 loads in flight
# speedup vs baseline: 1.0045x; 1.0045x over previous
; __device__ __forceinline__ void ph_ln1(const Params& p, int l, LAS unsigned char* lds, const int wvid) {
;     ...
;     __syncthreads();
;     for (int i = tid; i < D * NE / 4; i += NTHR) { const f32x4 w = *(const f32x4*)(p.in[I_ROUTW] + 4 * i); const int c = i >> 2, e0 = (i & 3) * 4;
;         rw[(e0 + 0) * D + c] = w[0]; rw[(e0 + 1) * D + c] = w[1]; rw[(e0 + 2) * D + c] = w[2]; rw[(e0 + 3) * D + c] = w[3]; }
;     if (tid < 16) lcnt[tid] = 0;
.LBB0_1066:
	s_or_b64 exec, exec, s[0:1]
	s_mov_b32 s4, s65
	s_mov_b64 s[18:19], s[66:67]
	s_waitcnt lgkmcnt(0)
	s_barrier
	v_mbcnt_lo_u32_b32 v34, -1, 0
	v_mbcnt_hi_u32_b32 v34, -1, v34
	s_nop 0
	v_or_b32_e32 v38, s75, v34
	v_cmp_gt_i32_e32 vcc, s70, v38
	s_barrier
	s_and_saveexec_b64 s[0:1], vcc
	v_readlane_b32 s48, v253, 62
	v_readlane_b32 s60, v254, 10
	v_readlane_b32 s61, v254, 11
	v_readlane_b32 s49, v253, 63
	v_readlane_b32 s50, v254, 0
	v_readlane_b32 s51, v254, 1
	v_readlane_b32 s52, v254, 2
	v_readlane_b32 s53, v254, 3
	v_readlane_b32 s54, v254, 4
	v_readlane_b32 s55, v254, 5
	v_readlane_b32 s56, v254, 6
	v_readlane_b32 s57, v254, 7
	v_readlane_b32 s58, v254, 8
	v_readlane_b32 s59, v254, 9
	v_readlane_b32 s62, v254, 12
	v_readlane_b32 s63, v254, 13
	s_cbranch_execz .LBB0_1069
	v_lshlrev_b32_e32 v0, 14, v38
	v_and_b32_e32 v3, 0xc000, v0
	v_and_b32_e32 v5, -4, v38
	v_add3_u32 v3, 0, v3, v5
	v_lshlrev_b32_e32 v2, 4, v38
	v_add_u32_e32 v184, 0x0, v2
	global_load_dwordx4 v[118:121], v184, s[60:61]
	v_add_u32_e32 v185, 0x2000, v2
	global_load_dwordx4 v[122:125], v185, s[60:61]
	v_add_u32_e32 v186, 0x4000, v2
	global_load_dwordx4 v[126:129], v186, s[60:61]
	v_add_u32_e32 v187, 0x6000, v2
	global_load_dwordx4 v[130:133], v187, s[60:61]
	v_add_u32_e32 v188, 0x8000, v2
	global_load_dwordx4 v[134:137], v188, s[60:61]
	v_add_u32_e32 v189, 0xa000, v2
	global_load_dwordx4 v[138:141], v189, s[60:61]
	v_add_u32_e32 v194, 0xc000, v2
	global_load_dwordx4 v[142:145], v194, s[60:61]
	v_add_u32_e32 v195, 0xe000, v2
	global_load_dwordx4 v[146:149], v195, s[60:61]
	s_waitcnt vmcnt(7)
	ds_write2st64_b32 v3, v118, v119 offset1:16
	ds_write2st64_b32 v3, v120, v121 offset0:32 offset1:48
	s_waitcnt vmcnt(6)
	ds_write2st64_b32 v3, v122, v123 offset0:2 offset1:18
	ds_write2st64_b32 v3, v124, v125 offset0:34 offset1:50
	s_waitcnt vmcnt(5)
	ds_write2st64_b32 v3, v126, v127 offset0:4 offset1:20
	ds_write2st64_b32 v3, v128, v129 offset0:36 offset1:52
	s_waitcnt vmcnt(4)
	ds_write2st64_b32 v3, v130, v131 offset0:6 offset1:22
	ds_write2st64_b32 v3, v132, v133 offset0:38 offset1:54
	s_waitcnt vmcnt(3)
	ds_write2st64_b32 v3, v134, v135 offset0:8 offset1:24
	ds_write2st64_b32 v3, v136, v137 offset0:40 offset1:56
	s_waitcnt vmcnt(2)
	ds_write2st64_b32 v3, v138, v139 offset0:10 offset1:26
	ds_write2st64_b32 v3, v140, v141 offset0:42 offset1:58
	s_waitcnt vmcnt(1)
	ds_write2st64_b32 v3, v142, v143 offset0:12 offset1:28
	ds_write2st64_b32 v3, v144, v145 offset0:44 offset1:60
	s_waitcnt vmcnt(0)
	ds_write2st64_b32 v3, v146, v147 offset0:14 offset1:30
	ds_write2st64_b32 v3, v148, v149 offset0:46 offset1:62
